# speedup vs baseline: 1.0103x; 1.0018x over previous
_Z12carry_kernelPKDv2_DF16_PDF16_:
	s_load_dwordx4 s[4:7], s[0:1], 0x0
	s_lshl_b32 s1, s2, 1
	s_mul_hi_u32 s3, s2, 0xaaaaaaab
	s_lshr_b32 s0, s2, 3
	s_and_b32 s1, s1, 12
	s_lshr_b32 s3, s3, 4
	s_add_i32 s1, s1, s3
	s_mul_hi_u32 s3, s0, 0x55555556
	s_mul_i32 s3, s3, 3
	s_sub_i32 s0, s0, s3
	s_mul_i32 s1, s1, 6
	s_lshl_b32 s0, s0, 1
	s_add_i32 s1, s1, s0
	s_and_b32 s0, s2, 1
	s_or_b32 s8, s1, s0
	s_mul_hi_u32 s0, s1, 0xaaaaaaab
	s_lshr_b32 s0, s0, 2
	s_bitcmp0_b32 s0, 1
	s_mov_b32 s9, 0
	s_cselect_b64 vcc, -1, 0
	s_lshl_b64 s[0:1], s[8:9], 17
	v_and_b32_e32 v1, 31, v0
	s_waitcnt lgkmcnt(0)
	s_add_u32 s0, s4, s0
	s_addc_u32 s1, s5, s1
	v_lshlrev_b32_e32 v2, 2, v1
	v_mov_b32_e32 v3, 0
	v_and_b32_e32 v56, 0x3e0, v0
	v_sub_u32_e32 v7, 0x3ff, v56
	v_cndmask_b32_e32 v7, v7, v56, vcc
	v_mov_b32_e32 v71, 0xffffff80
	v_mov_b32_e32 v72, 0x80
	v_cndmask_b32_e32 v71, v71, v72, vcc
	v_lshl_add_u32 v70, v7, 7, v2
	v_lshlrev_b32_e32 v90, 1, v1
	v_lshl_add_u32 v90, v7, 6, v90
	v_ashrrev_i32_e32 v91, 1, v71
	global_load_dword v69, v70, s[0:1]
	v_add_u32_e32 v70, v70, v71
	global_load_dword v68, v70, s[0:1]
	v_add_u32_e32 v70, v70, v71
	global_load_dword v67, v70, s[0:1]
	v_add_u32_e32 v70, v70, v71
	global_load_dword v66, v70, s[0:1]
	v_add_u32_e32 v70, v70, v71
	global_load_dword v65, v70, s[0:1]
	v_add_u32_e32 v70, v70, v71
	global_load_dword v64, v70, s[0:1]
	v_add_u32_e32 v70, v70, v71
	global_load_dword v63, v70, s[0:1]
	v_add_u32_e32 v70, v70, v71
	global_load_dword v62, v70, s[0:1]
	v_add_u32_e32 v70, v70, v71
	global_load_dword v61, v70, s[0:1]
	v_add_u32_e32 v70, v70, v71
	global_load_dword v60, v70, s[0:1]
	v_add_u32_e32 v70, v70, v71
	global_load_dword v59, v70, s[0:1]
	v_add_u32_e32 v70, v70, v71
	global_load_dword v58, v70, s[0:1]
	v_add_u32_e32 v70, v70, v71
	global_load_dword v25, v70, s[0:1]
	v_add_u32_e32 v70, v70, v71
	global_load_dword v24, v70, s[0:1]
	v_add_u32_e32 v70, v70, v71
	global_load_dword v23, v70, s[0:1]
	v_add_u32_e32 v70, v70, v71
	global_load_dword v22, v70, s[0:1]
	v_add_u32_e32 v70, v70, v71
	global_load_dword v21, v70, s[0:1]
	v_add_u32_e32 v70, v70, v71
	global_load_dword v20, v70, s[0:1]
	v_add_u32_e32 v70, v70, v71
	global_load_dword v19, v70, s[0:1]
	v_add_u32_e32 v70, v70, v71
	global_load_dword v18, v70, s[0:1]
	v_add_u32_e32 v70, v70, v71
	global_load_dword v17, v70, s[0:1]
	v_add_u32_e32 v70, v70, v71
	global_load_dword v16, v70, s[0:1]
	v_add_u32_e32 v70, v70, v71
	global_load_dword v15, v70, s[0:1]
	v_add_u32_e32 v70, v70, v71
	global_load_dword v14, v70, s[0:1]
	v_add_u32_e32 v70, v70, v71
	global_load_dword v13, v70, s[0:1]
	v_add_u32_e32 v70, v70, v71
	global_load_dword v12, v70, s[0:1]
	v_add_u32_e32 v70, v70, v71
	global_load_dword v11, v70, s[0:1]
	v_add_u32_e32 v70, v70, v71
	global_load_dword v10, v70, s[0:1]
	v_add_u32_e32 v70, v70, v71
	global_load_dword v9, v70, s[0:1]
	v_add_u32_e32 v70, v70, v71
	global_load_dword v8, v70, s[0:1]
	v_add_u32_e32 v70, v70, v71
	global_load_dword v6, v70, s[0:1]
	v_add_u32_e32 v70, v70, v71
	global_load_dword v4, v70, s[0:1]
	s_waitcnt vmcnt(31)
	s_waitcnt vmcnt(30)
	v_fma_mix_f32 v5, v69, v68, 0 op_sel_hi:[1,1,0]
	s_waitcnt vmcnt(29)
	v_fma_mix_f32 v5, v5, v67, 0 op_sel_hi:[0,1,0]
	v_lshrrev_b32_e32 v0, 5, v0
	s_movk_i32 s0, 0x84
	v_mad_u32_u24 v2, v0, s0, v2
	v_lshlrev_b32_e32 v0, 2, v0
	s_waitcnt vmcnt(28)
	v_fma_mix_f32 v5, v5, v66, 0 op_sel_hi:[0,1,0]
	s_waitcnt vmcnt(27)
	v_fma_mix_f32 v5, v5, v65, 0 op_sel_hi:[0,1,0]
	s_waitcnt vmcnt(26)
	v_fma_mix_f32 v5, v5, v64, 0 op_sel_hi:[0,1,0]
	s_waitcnt vmcnt(25)
	v_fma_mix_f32 v5, v5, v63, 0 op_sel_hi:[0,1,0]
	v_mad_u32_u24 v0, v1, s0, v0
	s_waitcnt vmcnt(24)
	v_fma_mix_f32 v5, v5, v62, 0 op_sel_hi:[0,1,0]
	s_waitcnt vmcnt(23)
	v_fma_mix_f32 v5, v5, v61, 0 op_sel_hi:[0,1,0]
	s_waitcnt vmcnt(22)
	v_fma_mix_f32 v5, v5, v60, 0 op_sel_hi:[0,1,0]
	s_waitcnt vmcnt(21)
	v_fma_mix_f32 v5, v5, v59, 0 op_sel_hi:[0,1,0]
	s_waitcnt vmcnt(20)
	v_fma_mix_f32 v5, v5, v58, 0 op_sel_hi:[0,1,0]
	s_waitcnt vmcnt(19)
	v_fma_mix_f32 v5, v5, v25, 0 op_sel_hi:[0,1,0]
	s_waitcnt vmcnt(18)
	v_fma_mix_f32 v5, v5, v24, 0 op_sel_hi:[0,1,0]
	s_waitcnt vmcnt(17)
	v_fma_mix_f32 v5, v5, v23, 0 op_sel_hi:[0,1,0]
	s_waitcnt vmcnt(16)
	v_fma_mix_f32 v5, v5, v22, 0 op_sel_hi:[0,1,0]
	s_waitcnt vmcnt(15)
	v_fma_mix_f32 v5, v5, v21, 0 op_sel_hi:[0,1,0]
	s_waitcnt vmcnt(14)
	v_fma_mix_f32 v5, v5, v20, 0 op_sel_hi:[0,1,0]
	s_waitcnt vmcnt(13)
	v_fma_mix_f32 v5, v5, v19, 0 op_sel_hi:[0,1,0]
	s_waitcnt vmcnt(12)
	v_fma_mix_f32 v5, v5, v18, 0 op_sel_hi:[0,1,0]
	s_waitcnt vmcnt(11)
	v_fma_mix_f32 v5, v5, v17, 0 op_sel_hi:[0,1,0]
	s_waitcnt vmcnt(10)
	v_fma_mix_f32 v5, v5, v16, 0 op_sel_hi:[0,1,0]
	s_waitcnt vmcnt(9)
	v_fma_mix_f32 v5, v5, v15, 0 op_sel_hi:[0,1,0]
	s_waitcnt vmcnt(8)
	v_fma_mix_f32 v5, v5, v14, 0 op_sel_hi:[0,1,0]
	s_waitcnt vmcnt(7)
	v_fma_mix_f32 v5, v5, v13, 0 op_sel_hi:[0,1,0]
	s_waitcnt vmcnt(6)
	v_fma_mix_f32 v5, v5, v12, 0 op_sel_hi:[0,1,0]
	s_waitcnt vmcnt(5)
	v_fma_mix_f32 v5, v5, v11, 0 op_sel_hi:[0,1,0]
	s_waitcnt vmcnt(4)
	v_fma_mix_f32 v5, v5, v10, 0 op_sel_hi:[0,1,0]
	v_fma_mix_f32 v57, v69, 0, v69 op_sel:[0,0,1] op_sel_hi:[1,0,1]
	s_waitcnt vmcnt(3)
	v_fma_mix_f32 v5, v5, v9, 0 op_sel_hi:[0,1,0]
	v_fma_mix_f32 v57, v57, v68, v68 op_sel:[0,0,1] op_sel_hi:[0,1,1]
	v_fma_mix_f32 v57, v57, v67, v67 op_sel:[0,0,1] op_sel_hi:[0,1,1]
	v_fma_mix_f32 v57, v57, v66, v66 op_sel:[0,0,1] op_sel_hi:[0,1,1]
	v_fma_mix_f32 v57, v57, v65, v65 op_sel:[0,0,1] op_sel_hi:[0,1,1]
	v_fma_mix_f32 v57, v57, v64, v64 op_sel:[0,0,1] op_sel_hi:[0,1,1]
	v_fma_mix_f32 v57, v57, v63, v63 op_sel:[0,0,1] op_sel_hi:[0,1,1]
	v_fma_mix_f32 v57, v57, v62, v62 op_sel:[0,0,1] op_sel_hi:[0,1,1]
	v_fma_mix_f32 v57, v57, v61, v61 op_sel:[0,0,1] op_sel_hi:[0,1,1]
	v_fma_mix_f32 v57, v57, v60, v60 op_sel:[0,0,1] op_sel_hi:[0,1,1]
	v_fma_mix_f32 v57, v57, v59, v59 op_sel:[0,0,1] op_sel_hi:[0,1,1]
	v_fma_mix_f32 v57, v57, v58, v58 op_sel:[0,0,1] op_sel_hi:[0,1,1]
	v_fma_mix_f32 v57, v57, v25, v25 op_sel:[0,0,1] op_sel_hi:[0,1,1]
	v_fma_mix_f32 v57, v57, v24, v24 op_sel:[0,0,1] op_sel_hi:[0,1,1]
	v_fma_mix_f32 v57, v57, v23, v23 op_sel:[0,0,1] op_sel_hi:[0,1,1]
	v_fma_mix_f32 v57, v57, v22, v22 op_sel:[0,0,1] op_sel_hi:[0,1,1]
	v_fma_mix_f32 v57, v57, v21, v21 op_sel:[0,0,1] op_sel_hi:[0,1,1]
	v_fma_mix_f32 v57, v57, v20, v20 op_sel:[0,0,1] op_sel_hi:[0,1,1]
	v_fma_mix_f32 v57, v57, v19, v19 op_sel:[0,0,1] op_sel_hi:[0,1,1]
	v_fma_mix_f32 v57, v57, v18, v18 op_sel:[0,0,1] op_sel_hi:[0,1,1]
	v_fma_mix_f32 v57, v57, v17, v17 op_sel:[0,0,1] op_sel_hi:[0,1,1]
	v_fma_mix_f32 v57, v57, v16, v16 op_sel:[0,0,1] op_sel_hi:[0,1,1]
	v_fma_mix_f32 v57, v57, v15, v15 op_sel:[0,0,1] op_sel_hi:[0,1,1]
	v_fma_mix_f32 v57, v57, v14, v14 op_sel:[0,0,1] op_sel_hi:[0,1,1]
	v_fma_mix_f32 v57, v57, v13, v13 op_sel:[0,0,1] op_sel_hi:[0,1,1]
	s_waitcnt vmcnt(2)
	v_fma_mix_f32 v5, v5, v8, 0 op_sel_hi:[0,1,0]
	v_fma_mix_f32 v57, v57, v12, v12 op_sel:[0,0,1] op_sel_hi:[0,1,1]
	s_waitcnt vmcnt(1)
	v_fma_mix_f32 v5, v5, v6, 0 op_sel_hi:[0,1,0]
	v_fma_mix_f32 v57, v57, v11, v11 op_sel:[0,0,1] op_sel_hi:[0,1,1]
	v_fma_mix_f32 v57, v57, v10, v10 op_sel:[0,0,1] op_sel_hi:[0,1,1]
	s_waitcnt vmcnt(0)
	v_fma_mix_f32 v5, v5, v4, 0 op_sel_hi:[0,1,0]
	v_fma_mix_f32 v57, v57, v9, v9 op_sel:[0,0,1] op_sel_hi:[0,1,1]
	v_fma_mix_f32 v57, v57, v8, v8 op_sel:[0,0,1] op_sel_hi:[0,1,1]
	v_fma_mix_f32 v57, v57, v6, v6 op_sel:[0,0,1] op_sel_hi:[0,1,1]
	v_fma_mix_f32 v4, v57, v4, v4 op_sel:[0,0,1] op_sel_hi:[0,1,1]
	ds_write_b32 v2, v5 offset:8448
	ds_write_b32 v2, v4 offset:4224
	v_mbcnt_lo_u32_b32 v4, -1, 0
	s_waitcnt lgkmcnt(0)
	s_barrier
	v_mbcnt_hi_u32_b32 v4, -1, v4
	ds_read_b32 v70, v0 offset:4224
	ds_read_b32 v71, v0 offset:8448
	v_and_b32_e32 v5, 0x60, v4
	v_add_u32_e32 v57, -1, v4
	v_cmp_lt_i32_e32 vcc, v57, v5
	v_add_u32_e32 v73, -2, v4
	v_cmp_lt_i32_e64 s[0:1], v73, v5
	v_cndmask_b32_e32 v57, v57, v4, vcc
	v_lshlrev_b32_e32 v57, 2, v57
	s_waitcnt lgkmcnt(1)
	ds_bpermute_b32 v72, v57, v70
	v_cmp_eq_u32_e32 vcc, 0, v1
	v_cndmask_b32_e64 v73, v73, v4, s[0:1]
	v_lshlrev_b32_e32 v73, 2, v73
	v_cmp_gt_u32_e64 s[0:1], 2, v1
	s_waitcnt lgkmcnt(0)
	v_fma_f32 v72, v71, v72, v70
	v_cndmask_b32_e32 v70, v72, v70, vcc
	ds_bpermute_b32 v72, v57, v71
	ds_bpermute_b32 v74, v73, v70
	s_waitcnt lgkmcnt(1)
	v_mul_f32_e32 v72, v71, v72
	v_cndmask_b32_e32 v71, v72, v71, vcc
	s_waitcnt lgkmcnt(0)
	v_fma_f32 v72, v71, v74, v70
	v_cndmask_b32_e64 v70, v72, v70, s[0:1]
	ds_bpermute_b32 v72, v73, v71
	v_add_u32_e32 v73, -4, v4
	v_cmp_lt_i32_e64 s[2:3], v73, v5
	s_waitcnt lgkmcnt(0)
	v_mul_f32_e32 v72, v71, v72
	v_cndmask_b32_e64 v73, v73, v4, s[2:3]
	v_lshlrev_b32_e32 v73, 2, v73
	ds_bpermute_b32 v74, v73, v70
	v_cndmask_b32_e64 v71, v72, v71, s[0:1]
	v_cmp_gt_u32_e64 s[0:1], 4, v1
	s_waitcnt lgkmcnt(0)
	v_fma_f32 v72, v71, v74, v70
	v_cndmask_b32_e64 v70, v72, v70, s[0:1]
	ds_bpermute_b32 v72, v73, v71
	v_add_u32_e32 v73, -8, v4
	v_cmp_lt_i32_e64 s[2:3], v73, v5
	s_waitcnt lgkmcnt(0)
	v_mul_f32_e32 v72, v71, v72
	v_cndmask_b32_e64 v73, v73, v4, s[2:3]
	v_lshlrev_b32_e32 v73, 2, v73
	ds_bpermute_b32 v74, v73, v70
	v_cndmask_b32_e64 v71, v72, v71, s[0:1]
	v_cmp_gt_u32_e64 s[0:1], 8, v1
	s_waitcnt lgkmcnt(0)
	v_fma_f32 v72, v71, v74, v70
	v_cndmask_b32_e64 v70, v72, v70, s[0:1]
	ds_bpermute_b32 v72, v73, v71
	v_add_u32_e32 v73, -16, v4
	v_cmp_lt_i32_e64 s[2:3], v73, v5
	s_waitcnt lgkmcnt(0)
	v_mul_f32_e32 v5, v71, v72
	v_cndmask_b32_e64 v4, v73, v4, s[2:3]
	v_lshlrev_b32_e32 v4, 2, v4
	ds_bpermute_b32 v4, v4, v70
	v_cndmask_b32_e64 v5, v5, v71, s[0:1]
	v_cmp_gt_u32_e64 s[0:1], 16, v1
	s_waitcnt lgkmcnt(0)
	v_fma_f32 v4, v5, v4, v70
	v_cndmask_b32_e64 v4, v4, v70, s[0:1]
	ds_bpermute_b32 v4, v57, v4
	s_lshl_b64 s[0:1], s[8:9], 16
	s_add_u32 s0, s6, s0
	s_addc_u32 s1, s7, s1
	s_waitcnt lgkmcnt(0)
	v_cndmask_b32_e64 v4, v4, 0, vcc
	ds_write_b32 v0, v4
	s_waitcnt lgkmcnt(0)
	s_barrier
	ds_read_b32 v57, v2
	s_waitcnt lgkmcnt(0)
	v_cvt_f16_f32_e32 v70, v57
	v_fma_mixlo_f16 v26, v57, v69, v69 op_sel:[0,0,1] op_sel_hi:[0,1,1]
	global_store_short v90, v70, s[0:1]
	v_add_u32_e32 v90, v90, v91
	global_store_short v90, v26, s[0:1]
	v_add_u32_e32 v90, v90, v91
	v_fma_mix_f32 v26, v57, v69, v69 op_sel:[0,0,1] op_sel_hi:[0,1,1]
	v_fma_mixlo_f16 v27, v26, v68, v68 op_sel:[0,0,1] op_sel_hi:[0,1,1]
	v_fma_mix_f32 v26, v26, v68, v68 op_sel:[0,0,1] op_sel_hi:[0,1,1]
	global_store_short v90, v27, s[0:1]
	v_add_u32_e32 v90, v90, v91
	v_fma_mixlo_f16 v27, v26, v67, v67 op_sel:[0,0,1] op_sel_hi:[0,1,1]
	v_fma_mix_f32 v26, v26, v67, v67 op_sel:[0,0,1] op_sel_hi:[0,1,1]
	global_store_short v90, v27, s[0:1]
	v_add_u32_e32 v90, v90, v91
	v_fma_mixlo_f16 v27, v26, v66, v66 op_sel:[0,0,1] op_sel_hi:[0,1,1]
	v_fma_mix_f32 v2, v26, v66, v66 op_sel:[0,0,1] op_sel_hi:[0,1,1]
	global_store_short v90, v27, s[0:1]
	v_add_u32_e32 v90, v90, v91
	v_fma_mix_f32 v26, v2, v65, v65 op_sel:[0,0,1] op_sel_hi:[0,1,1]
	v_fma_mixlo_f16 v27, v2, v65, v65 op_sel:[0,0,1] op_sel_hi:[0,1,1]
	global_store_short v90, v27, s[0:1]
	v_add_u32_e32 v90, v90, v91
	v_fma_mix_f32 v27, v26, v64, v64 op_sel:[0,0,1] op_sel_hi:[0,1,1]
	v_fma_mixlo_f16 v26, v26, v64, v64 op_sel:[0,0,1] op_sel_hi:[0,1,1]
	global_store_short v90, v26, s[0:1]
	v_add_u32_e32 v90, v90, v91
	v_fma_mix_f32 v26, v27, v63, v63 op_sel:[0,0,1] op_sel_hi:[0,1,1]
	v_fma_mixlo_f16 v27, v27, v63, v63 op_sel:[0,0,1] op_sel_hi:[0,1,1]
	global_store_short v90, v27, s[0:1]
	v_add_u32_e32 v90, v90, v91
	v_fma_mix_f32 v27, v26, v62, v62 op_sel:[0,0,1] op_sel_hi:[0,1,1]
	v_fma_mixlo_f16 v26, v26, v62, v62 op_sel:[0,0,1] op_sel_hi:[0,1,1]
	global_store_short v90, v26, s[0:1]
	v_add_u32_e32 v90, v90, v91
	v_fma_mix_f32 v26, v27, v61, v61 op_sel:[0,0,1] op_sel_hi:[0,1,1]
	v_fma_mixlo_f16 v27, v27, v61, v61 op_sel:[0,0,1] op_sel_hi:[0,1,1]
	global_store_short v90, v27, s[0:1]
	v_add_u32_e32 v90, v90, v91
	v_fma_mix_f32 v27, v26, v60, v60 op_sel:[0,0,1] op_sel_hi:[0,1,1]
	v_fma_mixlo_f16 v26, v26, v60, v60 op_sel:[0,0,1] op_sel_hi:[0,1,1]
	global_store_short v90, v26, s[0:1]
	v_add_u32_e32 v90, v90, v91
	v_fma_mix_f32 v26, v27, v59, v59 op_sel:[0,0,1] op_sel_hi:[0,1,1]
	v_fma_mixlo_f16 v27, v27, v59, v59 op_sel:[0,0,1] op_sel_hi:[0,1,1]
	global_store_short v90, v27, s[0:1]
	v_add_u32_e32 v90, v90, v91
	v_fma_mix_f32 v27, v26, v58, v58 op_sel:[0,0,1] op_sel_hi:[0,1,1]
	v_fma_mixlo_f16 v26, v26, v58, v58 op_sel:[0,0,1] op_sel_hi:[0,1,1]
	global_store_short v90, v26, s[0:1]
	v_add_u32_e32 v90, v90, v91
	v_fma_mix_f32 v26, v27, v25, v25 op_sel:[0,0,1] op_sel_hi:[0,1,1]
	v_fma_mixlo_f16 v25, v27, v25, v25 op_sel:[0,0,1] op_sel_hi:[0,1,1]
	global_store_short v90, v25, s[0:1]
	v_add_u32_e32 v90, v90, v91
	v_fma_mix_f32 v25, v26, v24, v24 op_sel:[0,0,1] op_sel_hi:[0,1,1]
	v_fma_mixlo_f16 v24, v26, v24, v24 op_sel:[0,0,1] op_sel_hi:[0,1,1]
	global_store_short v90, v24, s[0:1]
	v_add_u32_e32 v90, v90, v91
	v_fma_mix_f32 v24, v25, v23, v23 op_sel:[0,0,1] op_sel_hi:[0,1,1]
	v_fma_mixlo_f16 v23, v25, v23, v23 op_sel:[0,0,1] op_sel_hi:[0,1,1]
	global_store_short v90, v23, s[0:1]
	v_add_u32_e32 v90, v90, v91
	v_fma_mix_f32 v23, v24, v22, v22 op_sel:[0,0,1] op_sel_hi:[0,1,1]
	v_fma_mixlo_f16 v22, v24, v22, v22 op_sel:[0,0,1] op_sel_hi:[0,1,1]
	global_store_short v90, v22, s[0:1]
	v_add_u32_e32 v90, v90, v91
	v_fma_mix_f32 v22, v23, v21, v21 op_sel:[0,0,1] op_sel_hi:[0,1,1]
	v_fma_mixlo_f16 v21, v23, v21, v21 op_sel:[0,0,1] op_sel_hi:[0,1,1]
	global_store_short v90, v21, s[0:1]
	v_add_u32_e32 v90, v90, v91
	v_fma_mix_f32 v21, v22, v20, v20 op_sel:[0,0,1] op_sel_hi:[0,1,1]
	v_fma_mixlo_f16 v20, v22, v20, v20 op_sel:[0,0,1] op_sel_hi:[0,1,1]
	global_store_short v90, v20, s[0:1]
	v_add_u32_e32 v90, v90, v91
	v_fma_mix_f32 v20, v21, v19, v19 op_sel:[0,0,1] op_sel_hi:[0,1,1]
	v_fma_mixlo_f16 v19, v21, v19, v19 op_sel:[0,0,1] op_sel_hi:[0,1,1]
	global_store_short v90, v19, s[0:1]
	v_add_u32_e32 v90, v90, v91
	v_fma_mix_f32 v19, v20, v18, v18 op_sel:[0,0,1] op_sel_hi:[0,1,1]
	v_fma_mixlo_f16 v18, v20, v18, v18 op_sel:[0,0,1] op_sel_hi:[0,1,1]
	global_store_short v90, v18, s[0:1]
	v_add_u32_e32 v90, v90, v91
	v_fma_mix_f32 v18, v19, v17, v17 op_sel:[0,0,1] op_sel_hi:[0,1,1]
	v_fma_mixlo_f16 v17, v19, v17, v17 op_sel:[0,0,1] op_sel_hi:[0,1,1]
	global_store_short v90, v17, s[0:1]
	v_add_u32_e32 v90, v90, v91
	v_fma_mix_f32 v17, v18, v16, v16 op_sel:[0,0,1] op_sel_hi:[0,1,1]
	v_fma_mixlo_f16 v16, v18, v16, v16 op_sel:[0,0,1] op_sel_hi:[0,1,1]
	global_store_short v90, v16, s[0:1]
	v_add_u32_e32 v90, v90, v91
	v_fma_mix_f32 v16, v17, v15, v15 op_sel:[0,0,1] op_sel_hi:[0,1,1]
	v_fma_mixlo_f16 v15, v17, v15, v15 op_sel:[0,0,1] op_sel_hi:[0,1,1]
	global_store_short v90, v15, s[0:1]
	v_add_u32_e32 v90, v90, v91
	v_fma_mix_f32 v15, v16, v14, v14 op_sel:[0,0,1] op_sel_hi:[0,1,1]
	v_fma_mixlo_f16 v14, v16, v14, v14 op_sel:[0,0,1] op_sel_hi:[0,1,1]
	global_store_short v90, v14, s[0:1]
	v_add_u32_e32 v90, v90, v91
	v_fma_mix_f32 v14, v15, v13, v13 op_sel:[0,0,1] op_sel_hi:[0,1,1]
	v_fma_mixlo_f16 v13, v15, v13, v13 op_sel:[0,0,1] op_sel_hi:[0,1,1]
	global_store_short v90, v13, s[0:1]
	v_add_u32_e32 v90, v90, v91
	v_fma_mix_f32 v13, v14, v12, v12 op_sel:[0,0,1] op_sel_hi:[0,1,1]
	v_fma_mixlo_f16 v12, v14, v12, v12 op_sel:[0,0,1] op_sel_hi:[0,1,1]
	global_store_short v90, v12, s[0:1]
	v_add_u32_e32 v90, v90, v91
	v_fma_mix_f32 v12, v13, v11, v11 op_sel:[0,0,1] op_sel_hi:[0,1,1]
	v_fma_mixlo_f16 v11, v13, v11, v11 op_sel:[0,0,1] op_sel_hi:[0,1,1]
	global_store_short v90, v11, s[0:1]
	v_add_u32_e32 v90, v90, v91
	v_fma_mix_f32 v11, v12, v10, v10 op_sel:[0,0,1] op_sel_hi:[0,1,1]
	v_fma_mixlo_f16 v10, v12, v10, v10 op_sel:[0,0,1] op_sel_hi:[0,1,1]
	global_store_short v90, v10, s[0:1]
	v_add_u32_e32 v90, v90, v91
	v_fma_mix_f32 v10, v11, v9, v9 op_sel:[0,0,1] op_sel_hi:[0,1,1]
	v_fma_mixlo_f16 v9, v11, v9, v9 op_sel:[0,0,1] op_sel_hi:[0,1,1]
	global_store_short v90, v9, s[0:1]
	v_add_u32_e32 v90, v90, v91
	v_fma_mix_f32 v9, v10, v8, v8 op_sel:[0,0,1] op_sel_hi:[0,1,1]
	v_fma_mixlo_f16 v8, v10, v8, v8 op_sel:[0,0,1] op_sel_hi:[0,1,1]
	global_store_short v90, v8, s[0:1]
	v_add_u32_e32 v90, v90, v91
	v_fma_mixlo_f16 v4, v9, v6, v6 op_sel:[0,0,1] op_sel_hi:[0,1,1]
	global_store_short v90, v4, s[0:1]
	s_endpgm
